# q_route staircase top-16: each sorted-list insertion (16-deep dependent v_max/v_min chain) rewritten as one v_max plus independent v_med3_u32 (new L[i] = med3(L[i-1], L[i], x)); 513 fewer VALU instruc
# baseline (speedup 1.0000x reference)
; __device__ __forceinline__ uint32_t mono_key(float f) {
;   uint32_t u = __float_as_uint(f);
;   return (u & 0x80000000u) ? ~u : (u | 0x80000000u);
; }
; __device__ __forceinline__ void ins16(uint32_t (&Lk)[16], uint32_t x) {
; #pragma unroll
;   for (int i = 0; i < 16; ++i) { uint32_t hi = max(Lk[i], x); x = min(Lk[i], x); Lk[i] = hi; }
; __device__ void phase_q_route(KParams& p, int bid, int nb, char* smem) {
;     ...
;     float v1[16], v2[16];
; #pragma unroll
;     for (int r = 0; r < 16; ++r) { v1[r] = unmono_key(L1[r] & ~0x7Fu); v2[r] = unmono_key(L2[r] & ~0x7Fu); }
;     uint32_t C[16];
; #pragma unroll
;     for (int i = 0; i < 16; ++i) C[i] = 0u;
; #pragma unroll
;     for (int a = 0; a < 16; ++a)
; #pragma unroll
;       for (int bq = 0; bq < 16; ++bq)
;         if ((a + 1) * (bq + 1) <= 16) ins16(C, (mono_key(v1[a] + v2[bq]) & ~0xFFu) | (uint32_t)(a * 16 + bq));
.LBB0_1192:
	s_or_b64 exec, exec, s[48:49]
	v_cmp_lt_i32_e32 vcc, -1, v12
	v_and_b32_e32 v14, 0xffffff80, v12
	v_and_b32_e32 v17, 0xffffff80, v9
	v_cndmask_b32_e64 v12, v174, -1, vcc
	v_cmp_lt_i32_e32 vcc, -1, v9
	v_xor_b32_e32 v15, v12, v14
	v_and_b32_e32 v16, 0xffffff80, v10
	v_cndmask_b32_e64 v9, v174, -1, vcc
	v_cmp_lt_i32_e32 vcc, -1, v10
	v_xor_b32_e32 v14, v9, v17
	v_and_b32_e32 v35, 0xffffff80, v70
	v_cndmask_b32_e64 v9, v174, -1, vcc
	v_cmp_lt_i32_e32 vcc, -1, v70
	v_xor_b32_e32 v17, v9, v16
	v_and_b32_e32 v34, 0xffffff80, v2
	v_cndmask_b32_e64 v10, v174, -1, vcc
	v_cmp_lt_i32_e32 vcc, -1, v8
	v_xor_b32_e32 v16, v10, v35
	v_and_b32_e32 v31, 0xffffff80, v22
	v_cndmask_b32_e64 v9, v174, -1, vcc
	v_cmp_lt_i32_e32 vcc, -1, v7
	v_bitop3_b32 v12, v9, v8, s3 bitop3:0x78
	v_and_b32_e32 v32, 0xffffff80, v6
	v_cndmask_b32_e64 v8, v174, -1, vcc
	v_cmp_lt_i32_e32 vcc, -1, v23
	v_bitop3_b32 v10, v8, v7, s3 bitop3:0x78
	v_and_b32_e32 v33, 0xffffff80, v23
	v_cndmask_b32_e64 v7, v174, -1, vcc
	v_cmp_lt_i32_e32 vcc, -1, v2
	v_and_b32_e32 v46, 0xffffff80, v4
	v_and_b32_e32 v45, 0xffffff80, v18
	v_cndmask_b32_e64 v2, v174, -1, vcc
	v_cmp_lt_i32_e32 vcc, -1, v22
	v_xor_b32_e32 v8, v2, v34
	v_and_b32_e32 v42, 0xffffff80, v19
	v_cndmask_b32_e64 v2, v174, -1, vcc
	v_cmp_lt_i32_e32 vcc, -1, v6
	v_xor_b32_e32 v23, v2, v31
	v_and_b32_e32 v44, 0xffffff80, v66
	v_cndmask_b32_e64 v6, v174, -1, vcc
	v_cmp_lt_i32_e32 vcc, -1, v5
	v_xor_b32_e32 v22, v6, v32
	v_xor_b32_e32 v9, v7, v33
	v_cndmask_b32_e64 v2, v174, -1, vcc
	v_cmp_lt_i32_e32 vcc, -1, v24
	v_bitop3_b32 v2, v2, v5, s3 bitop3:0x78
	v_and_b32_e32 v50, 0xffffff80, v41
	v_cndmask_b32_e64 v5, v174, -1, vcc
	v_cmp_lt_i32_e32 vcc, -1, v3
	v_bitop3_b32 v24, v5, v24, s3 bitop3:0x78
	v_and_b32_e32 v51, 0xffffff80, v40
	v_cndmask_b32_e64 v5, v174, -1, vcc
	v_cmp_lt_i32_e32 vcc, -1, v25
	v_bitop3_b32 v3, v5, v3, s3 bitop3:0x78
	v_and_b32_e32 v52, 0xffffff80, v39
	v_cndmask_b32_e64 v5, v174, -1, vcc
	v_cmp_lt_i32_e32 vcc, -1, v18
	v_bitop3_b32 v43, v5, v25, s3 bitop3:0x78
	v_and_b32_e32 v53, 0xffffff80, v38
	v_cndmask_b32_e64 v5, v174, -1, vcc
	v_cmp_lt_i32_e32 vcc, -1, v4
	v_xor_b32_e32 v5, v5, v45
	v_and_b32_e32 v54, 0xffffff80, v37
	v_cndmask_b32_e64 v4, v174, -1, vcc
	v_cmp_lt_i32_e32 vcc, -1, v19
	v_xor_b32_e32 v4, v4, v46
	v_and_b32_e32 v55, 0xffffff80, v21
	v_cndmask_b32_e64 v6, v174, -1, vcc
	v_cmp_lt_i32_e32 vcc, -1, v66
	v_xor_b32_e32 v45, v6, v42
	v_mov_b32_e32 v6, v9
	v_cndmask_b32_e64 v7, v174, -1, vcc
	v_xor_b32_e32 v44, v7, v44
	v_mov_b32_e32 v7, v5
	v_pk_add_f32 v[18:19], v[44:45], v[6:7] op_sel_hi:[0,1]
	v_not_b32_e32 v25, v19
	v_or_b32_e32 v42, 0x80000000, v19
	v_cmp_gt_i32_e32 vcc, 0, v19
	v_and_b32_e32 v48, 0xffffff80, v20
	v_and_b32_e32 v49, 0xffffff80, v13
	v_cndmask_b32_e32 v19, v42, v25, vcc
	v_and_b32_e32 v25, 0xffffff00, v19
	v_not_b32_e32 v19, v18
	v_or_b32_e32 v42, 0x80000000, v18
	v_cmp_gt_i32_e32 vcc, 0, v18
	v_and_b32_e32 v35, 0xffffff80, v30
	v_and_b32_e32 v36, 0xffffff80, v29
	v_cndmask_b32_e32 v18, v42, v19, vcc
	v_and_or_b32 v42, v18, s47, 1
	v_mov_b32_e32 v18, v17
	v_mov_b32_e32 v19, v15
	v_pk_add_f32 v[46:47], v[44:45], v[18:19] op_sel_hi:[0,1]
	v_not_b32_e32 v58, v47
	v_or_b32_e32 v59, 0x80000000, v47
	v_cmp_gt_i32_e32 vcc, 0, v47
	v_max_u32_e32 v56, v25, v42
	v_min_u32_e32 v57, v25, v42
	v_cndmask_b32_e32 v47, v59, v58, vcc
	v_and_or_b32 v47, v47, s47, 2
	v_max_u32_e32 v58, v56, v47
	v_min_u32_e32 v56, v56, v47
	v_med3_u32 v25, v25, v42, v47
	v_not_b32_e32 v42, v46
	v_or_b32_e32 v47, 0x80000000, v46
	v_cmp_gt_i32_e32 vcc, 0, v46
	v_min_u32_e32 v59, v57, v56
	v_and_b32_e32 v33, 0xffffff80, v28
	v_cndmask_b32_e32 v42, v47, v42, vcc
	v_and_or_b32 v42, v42, s47, 3
	v_max_u32_e32 v60, v58, v42
	v_min_u32_e32 v42, v58, v42
	v_max_u32_e32 v58, v25, v42
	v_min_u32_e32 v61, v25, v42
	v_mov_b32_e32 v25, v23
	v_pk_add_f32 v[46:47], v[44:45], v[24:25] op_sel_hi:[0,1]
	v_med3_u32 v56, v57, v56, v42
	v_not_b32_e32 v42, v47
	v_or_b32_e32 v62, 0x80000000, v47
	v_cmp_gt_i32_e32 vcc, 0, v47
	v_min_u32_e32 v57, v59, v61
	v_and_b32_e32 v34, 0xffffff80, v27
	v_cndmask_b32_e32 v42, v62, v42, vcc
	v_and_or_b32 v47, v42, s47, 6
	v_not_b32_e32 v42, v46
	v_or_b32_e32 v62, 0x80000000, v46
	v_cmp_gt_i32_e32 vcc, 0, v46
	v_and_b32_e32 v31, 0xffffff80, v26
	v_and_b32_e32 v32, 0xffffff80, v11
	v_cndmask_b32_e32 v42, v62, v42, vcc
	v_cmp_lt_i32_e32 vcc, -1, v41
	v_and_or_b32 v46, v42, s47, 7
	s_nop 0
	v_cndmask_b32_e64 v41, v174, -1, vcc
	v_cmp_lt_i32_e32 vcc, -1, v40
	v_xor_b32_e32 v41, v41, v50
	s_nop 0
	v_cndmask_b32_e64 v40, v174, -1, vcc
	v_xor_b32_e32 v40, v40, v51
	v_pk_add_f32 v[40:41], v[44:45], v[40:41] op_sel_hi:[0,1]
	v_not_b32_e32 v42, v41
	v_or_b32_e32 v50, 0x80000000, v41
	v_cmp_gt_i32_e32 vcc, 0, v41
	s_nop 1
	v_cndmask_b32_e32 v41, v50, v42, vcc
	v_not_b32_e32 v42, v40
	v_or_b32_e32 v50, 0x80000000, v40
	v_cmp_gt_i32_e32 vcc, 0, v40
	v_and_or_b32 v41, v41, s47, 8
	s_nop 0
	v_cndmask_b32_e32 v40, v50, v42, vcc
	v_cmp_lt_i32_e32 vcc, -1, v39
	v_and_or_b32 v40, v40, s47, 9
	s_nop 0
	v_cndmask_b32_e64 v39, v174, -1, vcc
	v_cmp_lt_i32_e32 vcc, -1, v38
	v_xor_b32_e32 v39, v39, v52
	s_nop 0
	v_cndmask_b32_e64 v38, v174, -1, vcc
	v_xor_b32_e32 v38, v38, v53
	v_pk_add_f32 v[38:39], v[44:45], v[38:39] op_sel_hi:[0,1]
	v_not_b32_e32 v42, v39
	v_or_b32_e32 v50, 0x80000000, v39
	v_cmp_gt_i32_e32 vcc, 0, v39
	s_nop 1
	v_cndmask_b32_e32 v39, v50, v42, vcc
	v_and_or_b32 v50, v39, s47, 10
	v_not_b32_e32 v39, v38
	v_or_b32_e32 v42, 0x80000000, v38
	v_cmp_gt_i32_e32 vcc, 0, v38
	s_nop 1
	v_cndmask_b32_e32 v38, v42, v39, vcc
	v_cmp_lt_i32_e32 vcc, -1, v37
	v_and_or_b32 v51, v38, s47, 11
	v_mov_b32_e32 v42, v45
; __device__ __forceinline__ void ins16(uint32_t (&Lk)[16], uint32_t x) {
; #pragma unroll
;   for (int i = 0; i < 16; ++i) { uint32_t hi = max(Lk[i], x); x = min(Lk[i], x); Lk[i] = hi; }
; __device__ void phase_q_route(KParams& p, int bid, int nb, char* smem) {
;     ...
;     for (int a = 0; a < 16; ++a)
; #pragma unroll
;       for (int bq = 0; bq < 16; ++bq)
;         if ((a + 1) * (bq + 1) <= 16) ins16(C, (mono_key(v1[a] + v2[bq]) & ~0xFFu) | (uint32_t)(a * 16 + bq));
	v_cndmask_b32_e64 v37, v174, -1, vcc
	v_cmp_lt_i32_e32 vcc, -1, v21
	v_xor_b32_e32 v39, v37, v54
	s_nop 0
	v_cndmask_b32_e64 v21, v174, -1, vcc
	v_xor_b32_e32 v38, v21, v55
	v_pk_add_f32 v[38:39], v[44:45], v[38:39] op_sel_hi:[0,1]
	v_not_b32_e32 v21, v39
	v_or_b32_e32 v37, 0x80000000, v39
	v_cmp_gt_i32_e32 vcc, 0, v39
	v_or_b32_e32 v39, 0x80000000, v38
	s_nop 0
	v_cndmask_b32_e32 v21, v37, v21, vcc
	v_and_or_b32 v37, v21, s47, 12
	v_not_b32_e32 v21, v38
	v_cmp_gt_i32_e32 vcc, 0, v38
	s_nop 1
	v_cndmask_b32_e32 v21, v39, v21, vcc
	v_pk_add_f32 v[38:39], v[44:45], v[42:43] op_sel_hi:[0,1]
	v_and_or_b32 v52, v21, s47, 13
	v_not_b32_e32 v21, v39
	v_or_b32_e32 v42, 0x80000000, v39
	v_cmp_gt_i32_e32 vcc, 0, v39
	v_or_b32_e32 v39, 0x80000000, v38
	s_nop 0
	v_cndmask_b32_e32 v21, v42, v21, vcc
	v_and_or_b32 v42, v21, s47, 14
	v_not_b32_e32 v21, v38
	v_cmp_gt_i32_e32 vcc, 0, v38
	s_nop 1
	v_cndmask_b32_e32 v21, v39, v21, vcc
	v_pk_add_f32 v[38:39], v[22:23], v[6:7] op_sel_hi:[0,1]
	v_and_or_b32 v43, v21, s47, 15
	v_not_b32_e32 v21, v39
	v_or_b32_e32 v53, 0x80000000, v39
	v_cmp_gt_i32_e32 vcc, 0, v39
	v_or_b32_e32 v39, 0x80000000, v38
	s_nop 0
	v_cndmask_b32_e32 v21, v53, v21, vcc
	v_and_or_b32 v53, v21, s47, 16
	v_not_b32_e32 v21, v38
	v_cmp_gt_i32_e32 vcc, 0, v38
	s_nop 1
	v_cndmask_b32_e32 v21, v39, v21, vcc
	v_pk_add_f32 v[38:39], v[22:23], v[18:19] op_sel_hi:[0,1]
	v_and_or_b32 v54, v21, s47, 17
	v_not_b32_e32 v21, v39
	v_or_b32_e32 v55, 0x80000000, v39
	v_cmp_gt_i32_e32 vcc, 0, v39
	v_or_b32_e32 v39, 0x80000000, v38
	v_pk_add_f32 v[18:19], v[16:17], v[18:19] op_sel_hi:[0,1]
	v_cndmask_b32_e32 v21, v55, v21, vcc
	v_and_or_b32 v55, v21, s47, 18
	v_not_b32_e32 v21, v38
	v_cmp_gt_i32_e32 vcc, 0, v38
	s_nop 1
	v_cndmask_b32_e32 v21, v39, v21, vcc
	v_cmp_lt_i32_e32 vcc, -1, v20
	v_and_or_b32 v62, v21, s47, 19
	s_nop 0
	v_cndmask_b32_e64 v20, v174, -1, vcc
	v_cmp_lt_i32_e32 vcc, -1, v13
	v_xor_b32_e32 v21, v20, v48
	s_nop 0
	v_cndmask_b32_e64 v13, v174, -1, vcc
	v_xor_b32_e32 v20, v13, v49
	v_pk_add_f32 v[38:39], v[44:45], v[20:21] op_sel_hi:[0,1]
	v_not_b32_e32 v13, v39
	v_or_b32_e32 v44, 0x80000000, v39
	v_cmp_gt_i32_e32 vcc, 0, v39
	s_nop 1
	v_cndmask_b32_e32 v13, v44, v13, vcc
	v_and_or_b32 v13, v13, s47, 4
	v_max_u32_e32 v39, v60, v13
	v_med3_u32 v44, v60, v58, v13
	v_min_u32_e32 v13, v58, v13
	v_max_u32_e32 v45, v56, v13
	v_min_u32_e32 v48, v56, v13
	v_not_b32_e32 v56, v38
	v_or_b32_e32 v58, 0x80000000, v38
	v_cmp_gt_i32_e32 vcc, 0, v38
	v_med3_u32 v13, v59, v61, v13
	v_min_u32_e32 v49, v57, v48
	v_cndmask_b32_e32 v38, v58, v56, vcc
	v_and_or_b32 v38, v38, s47, 5
	v_max_u32_e32 v56, v39, v38
	v_med3_u32 v39, v39, v44, v38
	v_med3_u32 v44, v44, v45, v38
	v_min_u32_e32 v38, v45, v38
	v_max_u32_e32 v45, v13, v38
	v_min_u32_e32 v13, v13, v38
	v_med3_u32 v38, v57, v48, v38
	v_max_u32_e32 v57, v56, v47
	v_min_u32_e32 v47, v56, v47
	v_max_u32_e32 v56, v39, v47
	v_min_u32_e32 v39, v39, v47
	v_max_u32_e32 v47, v44, v39
	v_med3_u32 v44, v44, v45, v39
	v_min_u32_e32 v39, v45, v39
	v_min_u32_e32 v48, v49, v13
	v_med3_u32 v13, v49, v13, v39
	v_max_u32_e32 v49, v57, v46
	v_med3_u32 v57, v57, v56, v46
	v_med3_u32 v56, v56, v47, v46
	v_min_u32_e32 v46, v47, v46
	v_max_u32_e32 v45, v38, v39
	v_max_u32_e32 v47, v44, v46
	v_min_u32_e32 v44, v44, v46
	v_min_u32_e32 v38, v38, v39
	v_max_u32_e32 v46, v45, v44
	v_min_u32_e32 v44, v45, v44
	v_min_u32_e32 v39, v48, v38
	v_med3_u32 v38, v48, v38, v44
	v_max_u32_e32 v48, v49, v41
	v_med3_u32 v49, v49, v57, v41
	v_med3_u32 v57, v57, v56, v41
	v_med3_u32 v56, v56, v47, v41
	v_min_u32_e32 v41, v47, v41
	v_max_u32_e32 v45, v13, v44
	v_max_u32_e32 v47, v46, v41
	v_min_u32_e32 v41, v46, v41
	v_min_u32_e32 v13, v13, v44
	v_max_u32_e32 v46, v45, v41
	v_min_u32_e32 v41, v45, v41
	v_min_u32_e32 v44, v39, v13
	v_max_u32_e32 v45, v38, v41
	v_min_u32_e32 v38, v38, v41
	v_med3_u32 v13, v39, v13, v41
	v_max_u32_e32 v41, v48, v40
	v_med3_u32 v48, v48, v49, v40
	v_med3_u32 v49, v49, v57, v40
	v_med3_u32 v57, v57, v56, v40
	v_med3_u32 v56, v56, v47, v40
	v_med3_u32 v47, v47, v46, v40
	v_med3_u32 v46, v46, v45, v40
	v_min_u32_e32 v40, v45, v40
	v_min_u32_e32 v39, v44, v38
	v_med3_u32 v38, v44, v38, v40
	v_max_u32_e32 v44, v41, v50
	v_min_u32_e32 v41, v41, v50
	v_max_u32_e32 v50, v48, v41
	v_med3_u32 v48, v48, v49, v41
	v_med3_u32 v49, v49, v57, v41
	v_med3_u32 v57, v57, v56, v41
	v_med3_u32 v56, v56, v47, v41
	v_min_u32_e32 v41, v47, v41
	v_max_u32_e32 v45, v13, v40
	v_max_u32_e32 v47, v46, v41
	v_min_u32_e32 v41, v46, v41
	v_min_u32_e32 v13, v13, v40
	v_max_u32_e32 v46, v45, v41
	v_min_u32_e32 v41, v45, v41
	v_min_u32_e32 v40, v39, v13
	v_max_u32_e32 v45, v38, v41
	v_min_u32_e32 v38, v38, v41
	v_med3_u32 v13, v39, v13, v41
	v_max_u32_e32 v41, v44, v51
	v_min_u32_e32 v44, v44, v51
	v_max_u32_e32 v51, v50, v44
	v_med3_u32 v50, v50, v48, v44
	v_med3_u32 v48, v48, v49, v44
	v_med3_u32 v49, v49, v57, v44
	v_med3_u32 v57, v57, v56, v44
	v_med3_u32 v56, v56, v47, v44
	v_med3_u32 v47, v47, v46, v44
	v_med3_u32 v46, v46, v45, v44
	v_min_u32_e32 v44, v45, v44
	v_min_u32_e32 v39, v40, v38
	v_max_u32_e32 v45, v13, v44
	v_min_u32_e32 v13, v13, v44
	v_med3_u32 v38, v40, v38, v44
	v_max_u32_e32 v44, v41, v37
	v_med3_u32 v41, v41, v51, v37
	v_med3_u32 v51, v51, v50, v37
	v_med3_u32 v50, v50, v48, v37
	v_med3_u32 v48, v48, v49, v37
	v_med3_u32 v49, v49, v57, v37
	v_med3_u32 v57, v57, v56, v37
	v_med3_u32 v56, v56, v47, v37
	v_med3_u32 v47, v47, v46, v37
	v_med3_u32 v46, v46, v45, v37
	v_min_u32_e32 v37, v45, v37
	v_min_u32_e32 v40, v39, v13
	v_med3_u32 v13, v39, v13, v37
	v_max_u32_e32 v39, v44, v52
	v_min_u32_e32 v44, v44, v52
	v_max_u32_e32 v52, v41, v44
; __device__ __forceinline__ void ins16(uint32_t (&Lk)[16], uint32_t x) {
; #pragma unroll
;   for (int i = 0; i < 16; ++i) { uint32_t hi = max(Lk[i], x); x = min(Lk[i], x); Lk[i] = hi; }
; __device__ void phase_q_route(KParams& p, int bid, int nb, char* smem) {
;     ...
;     for (int a = 0; a < 16; ++a)
; #pragma unroll
;       for (int bq = 0; bq < 16; ++bq)
;         if ((a + 1) * (bq + 1) <= 16) ins16(C, (mono_key(v1[a] + v2[bq]) & ~0xFFu) | (uint32_t)(a * 16 + bq));
	v_min_u32_e32 v41, v41, v44
	v_max_u32_e32 v44, v51, v41
	v_med3_u32 v51, v51, v50, v41
	v_med3_u32 v50, v50, v48, v41
	v_med3_u32 v48, v48, v49, v41
	v_med3_u32 v49, v49, v57, v41
	v_med3_u32 v57, v57, v56, v41
	v_med3_u32 v56, v56, v47, v41
	v_min_u32_e32 v41, v47, v41
	v_max_u32_e32 v45, v38, v37
	v_max_u32_e32 v47, v46, v41
	v_min_u32_e32 v41, v46, v41
	v_min_u32_e32 v38, v38, v37
	v_max_u32_e32 v46, v45, v41
	v_min_u32_e32 v41, v45, v41
	v_min_u32_e32 v37, v40, v38
	v_max_u32_e32 v45, v13, v41
	v_min_u32_e32 v13, v13, v41
	v_med3_u32 v38, v40, v38, v41
	v_max_u32_e32 v41, v39, v42
	v_min_u32_e32 v39, v39, v42
	v_max_u32_e32 v42, v52, v39
	v_med3_u32 v52, v52, v44, v39
	v_med3_u32 v44, v44, v51, v39
	v_med3_u32 v51, v51, v50, v39
	v_med3_u32 v50, v50, v48, v39
	v_med3_u32 v48, v48, v49, v39
	v_med3_u32 v49, v49, v57, v39
	v_med3_u32 v57, v57, v56, v39
	v_med3_u32 v56, v56, v47, v39
	v_med3_u32 v47, v47, v46, v39
	v_med3_u32 v46, v46, v45, v39
	v_min_u32_e32 v39, v45, v39
	v_min_u32_e32 v40, v37, v13
	v_max_u32_e32 v45, v38, v39
	v_min_u32_e32 v38, v38, v39
	v_med3_u32 v13, v37, v13, v39
	v_max_u32_e32 v39, v41, v43
	v_min_u32_e32 v41, v41, v43
	v_max_u32_e32 v43, v42, v41
	v_med3_u32 v42, v42, v52, v41
	v_med3_u32 v52, v52, v44, v41
	v_med3_u32 v44, v44, v51, v41
	v_med3_u32 v51, v51, v50, v41
	v_med3_u32 v50, v50, v48, v41
	v_med3_u32 v48, v48, v49, v41
	v_med3_u32 v49, v49, v57, v41
	v_med3_u32 v57, v57, v56, v41
	v_med3_u32 v56, v56, v47, v41
	v_med3_u32 v47, v47, v46, v41
	v_med3_u32 v46, v46, v45, v41
	v_min_u32_e32 v41, v45, v41
	v_min_u32_e32 v37, v40, v38
	v_max_u32_e32 v45, v13, v41
	v_min_u32_e32 v13, v13, v41
	v_min_u32_e32 v13, v37, v13
	v_max_u32_e32 v37, v39, v53
	v_min_u32_e32 v39, v39, v53
	v_med3_u32 v38, v40, v38, v41
	v_max_u32_e32 v40, v43, v39
	v_med3_u32 v41, v43, v42, v39
	v_med3_u32 v42, v42, v52, v39
	v_med3_u32 v43, v52, v44, v39
	v_med3_u32 v44, v44, v51, v39
	v_med3_u32 v51, v51, v50, v39
	v_med3_u32 v50, v50, v48, v39
	v_med3_u32 v48, v48, v49, v39
	v_med3_u32 v49, v49, v57, v39
	v_med3_u32 v52, v57, v56, v39
	v_med3_u32 v53, v56, v47, v39
	v_med3_u32 v47, v47, v46, v39
	v_med3_u32 v46, v46, v45, v39
	v_min_u32_e32 v39, v45, v39
	v_max_u32_e32 v45, v38, v39
	v_min_u32_e32 v38, v38, v39
	v_max_u32_e32 v39, v37, v54
	v_min_u32_e32 v37, v37, v54
	v_max_u32_e32 v54, v40, v37
	v_med3_u32 v40, v40, v41, v37
	v_med3_u32 v41, v41, v42, v37
	v_med3_u32 v42, v42, v43, v37
	v_med3_u32 v43, v43, v44, v37
	v_med3_u32 v44, v44, v51, v37
	v_med3_u32 v51, v51, v50, v37
	v_med3_u32 v50, v50, v48, v37
	v_med3_u32 v48, v48, v49, v37
	v_med3_u32 v49, v49, v52, v37
	v_med3_u32 v52, v52, v53, v37
	v_med3_u32 v53, v53, v47, v37
	v_med3_u32 v47, v47, v46, v37
	v_med3_u32 v46, v46, v45, v37
	v_min_u32_e32 v37, v45, v37
	v_max3_u32 v13, v13, v38, v37
	v_min_u32_e32 v38, v39, v55
	v_max_u32_e32 v37, v39, v55
	v_max_u32_e32 v39, v54, v38
	v_med3_u32 v45, v54, v40, v38
	v_med3_u32 v40, v40, v41, v38
	v_med3_u32 v41, v41, v42, v38
	v_med3_u32 v42, v42, v43, v38
	v_med3_u32 v43, v43, v44, v38
	v_med3_u32 v44, v44, v51, v38
	v_med3_u32 v51, v51, v50, v38
	v_med3_u32 v50, v50, v48, v38
	v_med3_u32 v48, v48, v49, v38
	v_med3_u32 v49, v49, v52, v38
	v_med3_u32 v52, v52, v53, v38
	v_med3_u32 v53, v53, v47, v38
	v_med3_u32 v47, v47, v46, v38
	v_min_u32_e32 v38, v46, v38
	v_max_u32_e32 v46, v37, v62
	v_min_u32_e32 v37, v37, v62
	v_max_u32_e32 v54, v39, v37
	v_med3_u32 v55, v39, v45, v37
	v_med3_u32 v45, v45, v40, v37
	v_med3_u32 v40, v40, v41, v37
	v_med3_u32 v41, v41, v42, v37
	v_med3_u32 v42, v42, v43, v37
	v_med3_u32 v43, v43, v44, v37
	v_med3_u32 v44, v44, v51, v37
	v_med3_u32 v51, v51, v50, v37
	v_med3_u32 v50, v50, v48, v37
	v_med3_u32 v48, v48, v49, v37
	v_med3_u32 v49, v49, v52, v37
	v_med3_u32 v52, v52, v53, v37
	v_med3_u32 v53, v53, v47, v37
	v_min_u32_e32 v37, v47, v37
	v_max3_u32 v13, v13, v38, v37
	v_pk_add_f32 v[38:39], v[22:23], v[20:21] op_sel_hi:[0,1]
	v_not_b32_e32 v20, v39
	v_or_b32_e32 v37, 0x80000000, v39
	v_cmp_gt_i32_e32 vcc, 0, v39
	v_pk_add_f32 v[22:23], v[22:23], v[24:25] op_sel_hi:[0,1]
	v_or_b32_e32 v24, 0x80000000, v23
	v_cndmask_b32_e32 v20, v37, v20, vcc
	v_and_or_b32 v20, v20, s47, 20
	v_max_u32_e32 v37, v46, v20
	v_med3_u32 v39, v46, v54, v20
	v_med3_u32 v46, v54, v55, v20
	v_med3_u32 v47, v55, v45, v20
	v_med3_u32 v45, v45, v40, v20
	v_med3_u32 v40, v40, v41, v20
	v_med3_u32 v41, v41, v42, v20
	v_med3_u32 v42, v42, v43, v20
	v_med3_u32 v43, v43, v44, v20
	v_med3_u32 v44, v44, v51, v20
	v_med3_u32 v51, v51, v50, v20
	v_med3_u32 v50, v50, v48, v20
	v_med3_u32 v48, v48, v49, v20
	v_med3_u32 v49, v49, v52, v20
	v_med3_u32 v52, v52, v53, v20
	v_min_u32_e32 v20, v53, v20
	v_not_b32_e32 v53, v38
	v_or_b32_e32 v54, 0x80000000, v38
	v_cmp_gt_i32_e32 vcc, 0, v38
	s_nop 1
	v_cndmask_b32_e32 v38, v54, v53, vcc
	v_and_or_b32 v38, v38, s47, 21
	v_max_u32_e32 v53, v37, v38
	v_min_u32_e32 v37, v37, v38
	v_max_u32_e32 v38, v39, v37
	v_med3_u32 v39, v39, v46, v37
	v_med3_u32 v46, v46, v47, v37
	v_med3_u32 v47, v47, v45, v37
	v_med3_u32 v45, v45, v40, v37
	v_med3_u32 v40, v40, v41, v37
	v_med3_u32 v41, v41, v42, v37
	v_med3_u32 v42, v42, v43, v37
	v_med3_u32 v43, v43, v44, v37
	v_med3_u32 v44, v44, v51, v37
	v_med3_u32 v51, v51, v50, v37
	v_med3_u32 v50, v50, v48, v37
	v_med3_u32 v48, v48, v49, v37
	v_med3_u32 v49, v49, v52, v37
	v_min_u32_e32 v37, v52, v37
	v_max3_u32 v13, v13, v20, v37
	v_not_b32_e32 v20, v23
	v_cmp_gt_i32_e32 vcc, 0, v23
	s_nop 1
	v_cndmask_b32_e32 v20, v24, v20, vcc
	v_and_or_b32 v20, v20, s47, 22
	v_max_u32_e32 v23, v53, v20
	v_med3_u32 v24, v53, v38, v20
	v_med3_u32 v25, v38, v39, v20
	v_med3_u32 v37, v39, v46, v20
; __device__ __forceinline__ void ins16(uint32_t (&Lk)[16], uint32_t x) {
; #pragma unroll
;   for (int i = 0; i < 16; ++i) { uint32_t hi = max(Lk[i], x); x = min(Lk[i], x); Lk[i] = hi; }
; __device__ void phase_q_route(KParams& p, int bid, int nb, char* smem) {
;     ...
;     for (int a = 0; a < 16; ++a)
; #pragma unroll
;       for (int bq = 0; bq < 16; ++bq)
;         if ((a + 1) * (bq + 1) <= 16) ins16(C, (mono_key(v1[a] + v2[bq]) & ~0xFFu) | (uint32_t)(a * 16 + bq));
	v_med3_u32 v38, v46, v47, v20
	v_med3_u32 v39, v47, v45, v20
	v_med3_u32 v45, v45, v40, v20
	v_med3_u32 v40, v40, v41, v20
	v_med3_u32 v41, v41, v42, v20
	v_med3_u32 v42, v42, v43, v20
	v_med3_u32 v43, v43, v44, v20
	v_med3_u32 v44, v44, v51, v20
	v_med3_u32 v46, v51, v50, v20
	v_med3_u32 v47, v50, v48, v20
	v_med3_u32 v48, v48, v49, v20
	v_min_u32_e32 v20, v49, v20
	v_not_b32_e32 v49, v22
	v_or_b32_e32 v50, 0x80000000, v22
	v_cmp_gt_i32_e32 vcc, 0, v22
	s_nop 1
	v_cndmask_b32_e32 v22, v50, v49, vcc
	v_and_or_b32 v22, v22, s47, 23
	v_max_u32_e32 v49, v23, v22
	v_med3_u32 v50, v23, v24, v22
	v_med3_u32 v24, v24, v25, v22
	v_med3_u32 v25, v25, v37, v22
	v_med3_u32 v37, v37, v38, v22
	v_med3_u32 v38, v38, v39, v22
	v_med3_u32 v39, v39, v45, v22
	v_med3_u32 v45, v45, v40, v22
	v_med3_u32 v40, v40, v41, v22
	v_med3_u32 v41, v41, v42, v22
	v_med3_u32 v42, v42, v43, v22
	v_med3_u32 v43, v43, v44, v22
	v_med3_u32 v44, v44, v46, v22
	v_med3_u32 v46, v46, v47, v22
	v_med3_u32 v47, v47, v48, v22
	v_min_u32_e32 v22, v48, v22
	v_max3_u32 v13, v13, v20, v22
	v_pk_add_f32 v[22:23], v[16:17], v[6:7] op_sel_hi:[0,1]
	v_not_b32_e32 v20, v23
	v_or_b32_e32 v48, 0x80000000, v23
	v_cmp_gt_i32_e32 vcc, 0, v23
	s_nop 1
	v_cndmask_b32_e32 v20, v48, v20, vcc
	v_and_or_b32 v20, v20, s47, 32
	v_max_u32_e32 v23, v49, v20
	v_med3_u32 v48, v49, v50, v20
	v_med3_u32 v49, v50, v24, v20
	v_med3_u32 v24, v24, v25, v20
	v_med3_u32 v25, v25, v37, v20
	v_med3_u32 v37, v37, v38, v20
	v_med3_u32 v38, v38, v39, v20
	v_med3_u32 v39, v39, v45, v20
	v_med3_u32 v45, v45, v40, v20
	v_med3_u32 v40, v40, v41, v20
	v_med3_u32 v41, v41, v42, v20
	v_med3_u32 v42, v42, v43, v20
	v_med3_u32 v43, v43, v44, v20
	v_med3_u32 v44, v44, v46, v20
	v_med3_u32 v46, v46, v47, v20
	v_min_u32_e32 v20, v47, v20
	v_not_b32_e32 v47, v22
	v_or_b32_e32 v50, 0x80000000, v22
	v_cmp_gt_i32_e32 vcc, 0, v22
	s_nop 1
	v_cndmask_b32_e32 v22, v50, v47, vcc
	v_and_or_b32 v22, v22, s47, 33
	v_max_u32_e32 v47, v23, v22
	v_med3_u32 v23, v23, v48, v22
	v_med3_u32 v48, v48, v49, v22
	v_med3_u32 v49, v49, v24, v22
	v_med3_u32 v24, v24, v25, v22
	v_med3_u32 v25, v25, v37, v22
	v_med3_u32 v37, v37, v38, v22
	v_med3_u32 v38, v38, v39, v22
	v_med3_u32 v39, v39, v45, v22
	v_med3_u32 v45, v45, v40, v22
	v_med3_u32 v40, v40, v41, v22
	v_med3_u32 v41, v41, v42, v22
	v_med3_u32 v42, v42, v43, v22
	v_med3_u32 v43, v43, v44, v22
	v_med3_u32 v44, v44, v46, v22
	v_min_u32_e32 v22, v46, v22
	v_max3_u32 v13, v13, v20, v22
	v_not_b32_e32 v20, v19
	v_or_b32_e32 v22, 0x80000000, v19
	v_cmp_gt_i32_e32 vcc, 0, v19
	s_nop 1
	v_cndmask_b32_e32 v19, v22, v20, vcc
	v_and_or_b32 v19, v19, s47, 34
	v_max_u32_e32 v20, v47, v19
	v_med3_u32 v22, v47, v23, v19
	v_med3_u32 v23, v23, v48, v19
	v_med3_u32 v46, v48, v49, v19
	v_med3_u32 v47, v49, v24, v19
	v_med3_u32 v24, v24, v25, v19
	v_med3_u32 v25, v25, v37, v19
	v_med3_u32 v37, v37, v38, v19
	v_med3_u32 v38, v38, v39, v19
	v_med3_u32 v39, v39, v45, v19
	v_med3_u32 v45, v45, v40, v19
	v_med3_u32 v40, v40, v41, v19
	v_med3_u32 v41, v41, v42, v19
	v_med3_u32 v42, v42, v43, v19
	v_med3_u32 v43, v43, v44, v19
	v_min_u32_e32 v19, v44, v19
	v_not_b32_e32 v44, v18
	v_or_b32_e32 v48, 0x80000000, v18
	v_cmp_gt_i32_e32 vcc, 0, v18
	s_nop 1
	v_cndmask_b32_e32 v18, v48, v44, vcc
	v_and_or_b32 v18, v18, s47, 35
	v_max_u32_e32 v44, v20, v18
	v_med3_u32 v48, v20, v22, v18
	v_med3_u32 v22, v22, v23, v18
	v_med3_u32 v23, v23, v46, v18
	v_med3_u32 v46, v46, v47, v18
	v_med3_u32 v47, v47, v24, v18
	v_med3_u32 v24, v24, v25, v18
	v_med3_u32 v25, v25, v37, v18
	v_med3_u32 v37, v37, v38, v18
	v_med3_u32 v38, v38, v39, v18
	v_med3_u32 v39, v39, v45, v18
	v_med3_u32 v45, v45, v40, v18
	v_med3_u32 v40, v40, v41, v18
	v_med3_u32 v41, v41, v42, v18
	v_med3_u32 v42, v42, v43, v18
	v_min_u32_e32 v18, v43, v18
	v_max3_u32 v13, v13, v19, v18
	v_mov_b32_e32 v18, v14
	v_mov_b32_e32 v19, v16
	v_mov_b32_e32 v20, v5
	v_pk_add_f32 v[18:19], v[18:19], v[20:21]
	s_nop 0
	v_not_b32_e32 v16, v19
	v_or_b32_e32 v20, 0x80000000, v19
	v_cmp_gt_i32_e32 vcc, 0, v19
	s_nop 1
	v_cndmask_b32_e32 v16, v20, v16, vcc
	v_and_or_b32 v16, v16, s47, 36
	v_max_u32_e32 v19, v44, v16
	v_med3_u32 v20, v44, v48, v16
	v_med3_u32 v21, v48, v22, v16
	v_med3_u32 v22, v22, v23, v16
	v_med3_u32 v23, v23, v46, v16
	v_med3_u32 v43, v46, v47, v16
	v_med3_u32 v44, v47, v24, v16
	v_med3_u32 v24, v24, v25, v16
	v_med3_u32 v25, v25, v37, v16
	v_med3_u32 v37, v37, v38, v16
	v_med3_u32 v38, v38, v39, v16
	v_med3_u32 v39, v39, v45, v16
	v_med3_u32 v45, v45, v40, v16
	v_med3_u32 v40, v40, v41, v16
	v_med3_u32 v41, v41, v42, v16
	v_min_u32_e32 v16, v42, v16
	v_not_b32_e32 v42, v18
	v_or_b32_e32 v46, 0x80000000, v18
	v_cmp_gt_i32_e32 vcc, 0, v18
	s_nop 1
	v_cndmask_b32_e32 v18, v46, v42, vcc
	v_and_or_b32 v18, v18, s47, 48
	v_max_u32_e32 v42, v19, v18
	v_med3_u32 v46, v19, v20, v18
	v_med3_u32 v47, v20, v21, v18
	v_med3_u32 v48, v21, v22, v18
	v_med3_u32 v22, v22, v23, v18
	v_med3_u32 v23, v23, v43, v18
	v_med3_u32 v43, v43, v44, v18
	v_med3_u32 v44, v44, v24, v18
	v_med3_u32 v24, v24, v25, v18
	v_med3_u32 v25, v25, v37, v18
	v_med3_u32 v37, v37, v38, v18
	v_med3_u32 v38, v38, v39, v18
	v_med3_u32 v39, v39, v45, v18
	v_med3_u32 v45, v45, v40, v18
	v_med3_u32 v40, v40, v41, v18
	v_min_u32_e32 v18, v41, v18
	v_max3_u32 v13, v13, v16, v18
	v_mov_b32_e32 v18, v15
	v_mov_b32_e32 v19, v9
	v_pk_add_f32 v[20:21], v[14:15], v[18:19] op_sel_hi:[0,1]
	v_not_b32_e32 v15, v21
	v_or_b32_e32 v16, 0x80000000, v21
	v_cmp_gt_i32_e32 vcc, 0, v21
	v_pk_add_f32 v[8:9], v[8:9], v[6:7] op_sel_hi:[0,1]
	s_nop 0
	v_cndmask_b32_e32 v15, v16, v15, vcc
	v_and_or_b32 v15, v15, s47, 49
	v_max_u32_e32 v16, v42, v15
; __device__ __forceinline__ void ins16(uint32_t (&Lk)[16], uint32_t x) {
; #pragma unroll
;   for (int i = 0; i < 16; ++i) { uint32_t hi = max(Lk[i], x); x = min(Lk[i], x); Lk[i] = hi; }
; __device__ void phase_q_route(KParams& p, int bid, int nb, char* smem) {
;     ...
;     for (int a = 0; a < 16; ++a)
; #pragma unroll
;       for (int bq = 0; bq < 16; ++bq)
;         if ((a + 1) * (bq + 1) <= 16) ins16(C, (mono_key(v1[a] + v2[bq]) & ~0xFFu) | (uint32_t)(a * 16 + bq));
	v_med3_u32 v21, v42, v46, v15
	v_med3_u32 v41, v46, v47, v15
	v_med3_u32 v42, v47, v48, v15
	v_med3_u32 v46, v48, v22, v15
	v_med3_u32 v22, v22, v23, v15
	v_med3_u32 v23, v23, v43, v15
	v_med3_u32 v43, v43, v44, v15
	v_med3_u32 v44, v44, v24, v15
	v_med3_u32 v24, v24, v25, v15
	v_med3_u32 v25, v25, v37, v15
	v_med3_u32 v37, v37, v38, v15
	v_med3_u32 v38, v38, v39, v15
	v_med3_u32 v39, v39, v45, v15
	v_med3_u32 v45, v45, v40, v15
	v_min_u32_e32 v15, v40, v15
	v_not_b32_e32 v40, v20
	v_or_b32_e32 v47, 0x80000000, v20
	v_cmp_gt_i32_e32 vcc, 0, v20
	s_nop 1
	v_cndmask_b32_e32 v20, v47, v40, vcc
	v_and_or_b32 v20, v20, s47, 50
	v_max_u32_e32 v40, v16, v20
	v_min_u32_e32 v16, v16, v20
	v_max_u32_e32 v20, v21, v16
	v_med3_u32 v21, v21, v41, v16
	v_med3_u32 v41, v41, v42, v16
	v_med3_u32 v42, v42, v46, v16
	v_med3_u32 v46, v46, v22, v16
	v_med3_u32 v22, v22, v23, v16
	v_med3_u32 v23, v23, v43, v16
	v_med3_u32 v43, v43, v44, v16
	v_med3_u32 v44, v44, v24, v16
	v_med3_u32 v24, v24, v25, v16
	v_med3_u32 v25, v25, v37, v16
	v_med3_u32 v37, v37, v38, v16
	v_med3_u32 v38, v38, v39, v16
	v_med3_u32 v39, v39, v45, v16
	v_min_u32_e32 v16, v45, v16
	v_max3_u32 v45, v13, v15, v16
	v_mov_b32_e32 v13, v14
	v_mov_b32_e32 v16, v5
	v_pk_add_f32 v[14:15], v[12:13], v[16:17]
	s_nop 0
	v_not_b32_e32 v13, v15
	v_or_b32_e32 v16, 0x80000000, v15
	v_cmp_gt_i32_e32 vcc, 0, v15
	s_nop 1
	v_cndmask_b32_e32 v13, v16, v13, vcc
	v_and_or_b32 v13, v13, s47, 51
	v_max_u32_e32 v15, v40, v13
	v_med3_u32 v16, v40, v20, v13
	v_med3_u32 v17, v20, v21, v13
	v_med3_u32 v20, v21, v41, v13
	v_med3_u32 v21, v41, v42, v13
	v_med3_u32 v40, v42, v46, v13
	v_med3_u32 v41, v46, v22, v13
	v_med3_u32 v22, v22, v23, v13
	v_med3_u32 v23, v23, v43, v13
	v_med3_u32 v42, v43, v44, v13
	v_med3_u32 v43, v44, v24, v13
	v_med3_u32 v24, v24, v25, v13
	v_med3_u32 v25, v25, v37, v13
	v_med3_u32 v37, v37, v38, v13
	v_med3_u32 v38, v38, v39, v13
	v_min_u32_e32 v13, v39, v13
	v_not_b32_e32 v39, v14
	v_or_b32_e32 v44, 0x80000000, v14
	v_cmp_gt_i32_e32 vcc, 0, v14
	s_nop 1
	v_cndmask_b32_e32 v14, v44, v39, vcc
	v_and_or_b32 v14, v14, s47, 64
	v_max_u32_e32 v39, v15, v14
	v_med3_u32 v15, v15, v16, v14
	v_med3_u32 v16, v16, v17, v14
	v_med3_u32 v17, v17, v20, v14
	v_med3_u32 v20, v20, v21, v14
	v_med3_u32 v21, v21, v40, v14
	v_med3_u32 v40, v40, v41, v14
	v_med3_u32 v41, v41, v22, v14
	v_med3_u32 v22, v22, v23, v14
	v_med3_u32 v23, v23, v42, v14
	v_med3_u32 v42, v42, v43, v14
	v_med3_u32 v43, v43, v24, v14
	v_med3_u32 v24, v24, v25, v14
	v_med3_u32 v25, v25, v37, v14
	v_med3_u32 v37, v37, v38, v14
	v_min_u32_e32 v14, v38, v14
	v_max3_u32 v14, v45, v13, v14
	v_pk_add_f32 v[12:13], v[12:13], v[18:19] op_sel_hi:[0,1]
	v_not_b32_e32 v18, v13
	v_or_b32_e32 v19, 0x80000000, v13
	v_cmp_gt_i32_e32 vcc, 0, v13
	s_nop 1
	v_cndmask_b32_e32 v13, v19, v18, vcc
	v_and_b32_e32 v13, 0xffffff00, v13
	v_or_b32_e32 v13, 0x41, v13
	v_max_u32_e32 v18, v39, v13
	v_med3_u32 v19, v39, v15, v13
	v_med3_u32 v15, v15, v16, v13
	v_med3_u32 v16, v16, v17, v13
	v_med3_u32 v17, v17, v20, v13
	v_med3_u32 v20, v20, v21, v13
	v_med3_u32 v21, v21, v40, v13
	v_med3_u32 v38, v40, v41, v13
	v_med3_u32 v39, v41, v22, v13
	v_med3_u32 v22, v22, v23, v13
	v_med3_u32 v23, v23, v42, v13
	v_med3_u32 v40, v42, v43, v13
	v_med3_u32 v41, v43, v24, v13
	v_med3_u32 v24, v24, v25, v13
	v_med3_u32 v25, v25, v37, v13
	v_min_u32_e32 v13, v37, v13
	v_not_b32_e32 v37, v12
	v_or_b32_e32 v42, 0x80000000, v12
	v_cmp_gt_i32_e32 vcc, 0, v12
	s_nop 1
	v_cndmask_b32_e32 v12, v42, v37, vcc
	v_and_b32_e32 v12, 0xffffff00, v12
	v_or_b32_e32 v12, 0x42, v12
	v_max_u32_e32 v37, v18, v12
	v_med3_u32 v18, v18, v19, v12
	v_med3_u32 v19, v19, v15, v12
	v_med3_u32 v15, v15, v16, v12
	v_med3_u32 v16, v16, v17, v12
	v_med3_u32 v17, v17, v20, v12
	v_med3_u32 v20, v20, v21, v12
	v_med3_u32 v21, v21, v38, v12
	v_med3_u32 v38, v38, v39, v12
	v_med3_u32 v39, v39, v22, v12
	v_med3_u32 v22, v22, v23, v12
	v_med3_u32 v23, v23, v40, v12
	v_med3_u32 v40, v40, v41, v12
	v_med3_u32 v41, v41, v24, v12
	v_med3_u32 v24, v24, v25, v12
	v_min_u32_e32 v12, v25, v12
	v_max3_u32 v14, v14, v13, v12
	v_pk_add_f32 v[12:13], v[10:11], v[6:7] op_sel_hi:[0,1]
	v_not_b32_e32 v10, v13
	v_or_b32_e32 v25, 0x80000000, v13
	v_cmp_gt_i32_e32 vcc, 0, v13
	v_pk_add_f32 v[6:7], v[2:3], v[6:7] op_sel_hi:[0,1]
	v_not_b32_e32 v2, v7
	v_cndmask_b32_e32 v10, v25, v10, vcc
	v_and_b32_e32 v10, 0xffffff00, v10
	v_or_b32_e32 v10, 0x50, v10
	v_max_u32_e32 v13, v37, v10
	v_med3_u32 v25, v37, v18, v10
	v_med3_u32 v18, v18, v19, v10
	v_med3_u32 v19, v19, v15, v10
	v_med3_u32 v15, v15, v16, v10
	v_med3_u32 v16, v16, v17, v10
	v_med3_u32 v17, v17, v20, v10
	v_med3_u32 v20, v20, v21, v10
	v_med3_u32 v21, v21, v38, v10
	v_med3_u32 v37, v38, v39, v10
	v_med3_u32 v38, v39, v22, v10
	v_med3_u32 v22, v22, v23, v10
	v_med3_u32 v23, v23, v40, v10
	v_med3_u32 v39, v40, v41, v10
	v_med3_u32 v40, v41, v24, v10
	v_min_u32_e32 v10, v24, v10
	v_not_b32_e32 v24, v12
	v_or_b32_e32 v41, 0x80000000, v12
	v_cmp_gt_i32_e32 vcc, 0, v12
	s_nop 1
	v_cndmask_b32_e32 v12, v41, v24, vcc
	v_and_b32_e32 v12, 0xffffff00, v12
	v_or_b32_e32 v12, 0x51, v12
	v_max_u32_e32 v24, v13, v12
	v_med3_u32 v13, v13, v25, v12
	v_med3_u32 v25, v25, v18, v12
	v_med3_u32 v18, v18, v19, v12
	v_med3_u32 v19, v19, v15, v12
	v_med3_u32 v15, v15, v16, v12
	v_med3_u32 v16, v16, v17, v12
	v_med3_u32 v17, v17, v20, v12
	v_med3_u32 v20, v20, v21, v12
	v_med3_u32 v21, v21, v37, v12
	v_med3_u32 v37, v37, v38, v12
	v_med3_u32 v38, v38, v22, v12
	v_med3_u32 v22, v22, v23, v12
	v_med3_u32 v23, v23, v39, v12
	v_med3_u32 v39, v39, v40, v12
	v_min_u32_e32 v12, v40, v12
	v_max3_u32 v10, v14, v10, v12
; __device__ __forceinline__ void ins16(uint32_t (&Lk)[16], uint32_t x) {
; #pragma unroll
;   for (int i = 0; i < 16; ++i) { uint32_t hi = max(Lk[i], x); x = min(Lk[i], x); Lk[i] = hi; }
; __device__ void phase_q_route(KParams& p, int bid, int nb, char* smem) {
;     ...
;     for (int a = 0; a < 16; ++a)
; #pragma unroll
;       for (int bq = 0; bq < 16; ++bq)
;         if ((a + 1) * (bq + 1) <= 16) ins16(C, (mono_key(v1[a] + v2[bq]) & ~0xFFu) | (uint32_t)(a * 16 + bq));
	v_not_b32_e32 v12, v9
	v_or_b32_e32 v14, 0x80000000, v9
	v_cmp_gt_i32_e32 vcc, 0, v9
	s_nop 1
	v_cndmask_b32_e32 v9, v14, v12, vcc
	v_and_b32_e32 v9, 0xffffff00, v9
	v_or_b32_e32 v9, 0x60, v9
	v_max_u32_e32 v12, v24, v9
	v_med3_u32 v14, v24, v13, v9
	v_med3_u32 v13, v13, v25, v9
	v_med3_u32 v24, v25, v18, v9
	v_med3_u32 v18, v18, v19, v9
	v_med3_u32 v19, v19, v15, v9
	v_med3_u32 v15, v15, v16, v9
	v_med3_u32 v16, v16, v17, v9
	v_med3_u32 v17, v17, v20, v9
	v_med3_u32 v20, v20, v21, v9
	v_med3_u32 v21, v21, v37, v9
	v_med3_u32 v25, v37, v38, v9
	v_med3_u32 v37, v38, v22, v9
	v_med3_u32 v22, v22, v23, v9
	v_med3_u32 v23, v23, v39, v9
	v_min_u32_e32 v9, v39, v9
	v_not_b32_e32 v38, v8
	v_or_b32_e32 v39, 0x80000000, v8
	v_cmp_gt_i32_e32 vcc, 0, v8
	s_nop 1
	v_cndmask_b32_e32 v8, v39, v38, vcc
	v_and_b32_e32 v8, 0xffffff00, v8
	v_or_b32_e32 v8, 0x61, v8
	v_max_u32_e32 v38, v12, v8
	v_med3_u32 v12, v12, v14, v8
	v_med3_u32 v14, v14, v13, v8
	v_med3_u32 v13, v13, v24, v8
	v_med3_u32 v24, v24, v18, v8
	v_med3_u32 v18, v18, v19, v8
	v_med3_u32 v19, v19, v15, v8
	v_med3_u32 v15, v15, v16, v8
	v_med3_u32 v16, v16, v17, v8
	v_med3_u32 v17, v17, v20, v8
	v_med3_u32 v20, v20, v21, v8
	v_med3_u32 v21, v21, v25, v8
	v_med3_u32 v25, v25, v37, v8
	v_med3_u32 v37, v37, v22, v8
	v_med3_u32 v22, v22, v23, v8
	v_min_u32_e32 v8, v23, v8
	v_max3_u32 v8, v10, v9, v8
	v_or_b32_e32 v9, 0x80000000, v7
	v_cmp_gt_i32_e32 vcc, 0, v7
	s_nop 1
	v_cndmask_b32_e32 v2, v9, v2, vcc
	v_and_b32_e32 v2, 0xffffff00, v2
	v_or_b32_e32 v2, 0x70, v2
	v_max_u32_e32 v7, v38, v2
	v_med3_u32 v9, v38, v12, v2
	v_med3_u32 v10, v12, v14, v2
	v_med3_u32 v12, v14, v13, v2
	v_med3_u32 v13, v13, v24, v2
	v_med3_u32 v14, v24, v18, v2
	v_med3_u32 v18, v18, v19, v2
	v_med3_u32 v19, v19, v15, v2
	v_med3_u32 v15, v15, v16, v2
	v_med3_u32 v16, v16, v17, v2
	v_med3_u32 v17, v17, v20, v2
	v_med3_u32 v20, v20, v21, v2
	v_med3_u32 v21, v21, v25, v2
	v_med3_u32 v23, v25, v37, v2
	v_med3_u32 v24, v37, v22, v2
	v_min_u32_e32 v2, v22, v2
	v_not_b32_e32 v22, v6
	v_or_b32_e32 v25, 0x80000000, v6
	v_cmp_gt_i32_e32 vcc, 0, v6
	s_nop 1
	v_cndmask_b32_e32 v6, v25, v22, vcc
	v_and_b32_e32 v6, 0xffffff00, v6
	v_or_b32_e32 v6, 0x71, v6
	v_max_u32_e32 v22, v7, v6
	v_med3_u32 v25, v7, v9, v6
	v_med3_u32 v9, v9, v10, v6
	v_med3_u32 v10, v10, v12, v6
	v_med3_u32 v12, v12, v13, v6
	v_med3_u32 v13, v13, v14, v6
	v_med3_u32 v14, v14, v18, v6
	v_med3_u32 v18, v18, v19, v6
	v_med3_u32 v19, v19, v15, v6
	v_med3_u32 v15, v15, v16, v6
	v_med3_u32 v16, v16, v17, v6
	v_med3_u32 v17, v17, v20, v6
	v_med3_u32 v20, v20, v21, v6
	v_med3_u32 v21, v21, v23, v6
	v_med3_u32 v23, v23, v24, v6
	v_min_u32_e32 v6, v24, v6
	v_cmp_lt_i32_e32 vcc, -1, v30
	v_max3_u32 v2, v8, v2, v6
	s_nop 0
	v_cndmask_b32_e64 v6, v174, -1, vcc
	v_cmp_lt_i32_e32 vcc, -1, v29
	v_xor_b32_e32 v7, v6, v35
	s_nop 0
	v_cndmask_b32_e64 v8, v174, -1, vcc
	v_xor_b32_e32 v6, v8, v36
	v_pk_add_f32 v[6:7], v[4:5], v[6:7] op_sel:[1,0]
	s_nop 0
	v_not_b32_e32 v8, v7
	v_or_b32_e32 v24, 0x80000000, v7
	v_cmp_gt_i32_e32 vcc, 0, v7
	s_nop 1
	v_cndmask_b32_e32 v7, v24, v8, vcc
	v_and_b32_e32 v7, 0xffffff00, v7
	v_or_b32_e32 v7, 0x80, v7
	v_max_u32_e32 v8, v22, v7
	v_med3_u32 v22, v22, v25, v7
	v_med3_u32 v24, v25, v9, v7
	v_med3_u32 v9, v9, v10, v7
	v_med3_u32 v10, v10, v12, v7
	v_med3_u32 v12, v12, v13, v7
	v_med3_u32 v13, v13, v14, v7
	v_med3_u32 v14, v14, v18, v7
	v_med3_u32 v18, v18, v19, v7
	v_med3_u32 v19, v19, v15, v7
	v_med3_u32 v15, v15, v16, v7
	v_med3_u32 v16, v16, v17, v7
	v_med3_u32 v17, v17, v20, v7
	v_med3_u32 v20, v20, v21, v7
	v_med3_u32 v21, v21, v23, v7
	v_min_u32_e32 v7, v23, v7
	v_not_b32_e32 v23, v6
	v_or_b32_e32 v25, 0x80000000, v6
	v_cmp_gt_i32_e32 vcc, 0, v6
	s_nop 1
	v_cndmask_b32_e32 v6, v25, v23, vcc
	v_and_b32_e32 v6, 0xffffff00, v6
	v_or_b32_e32 v6, 0x90, v6
	v_max_u32_e32 v23, v8, v6
	v_med3_u32 v8, v8, v22, v6
	v_med3_u32 v22, v22, v24, v6
	v_med3_u32 v24, v24, v9, v6
	v_med3_u32 v9, v9, v10, v6
	v_med3_u32 v10, v10, v12, v6
	v_med3_u32 v12, v12, v13, v6
	v_med3_u32 v13, v13, v14, v6
	v_med3_u32 v14, v14, v18, v6
	v_med3_u32 v18, v18, v19, v6
	v_med3_u32 v19, v19, v15, v6
	v_med3_u32 v15, v15, v16, v6
	v_med3_u32 v16, v16, v17, v6
	v_med3_u32 v17, v17, v20, v6
	v_med3_u32 v20, v20, v21, v6
	v_min_u32_e32 v6, v21, v6
	v_cmp_lt_i32_e32 vcc, -1, v28
	v_max3_u32 v2, v2, v7, v6
	s_nop 0
	v_cndmask_b32_e64 v6, v174, -1, vcc
	v_cmp_lt_i32_e32 vcc, -1, v27
	v_xor_b32_e32 v7, v6, v33
	s_nop 0
	v_cndmask_b32_e64 v21, v174, -1, vcc
	v_xor_b32_e32 v6, v21, v34
	v_pk_add_f32 v[6:7], v[4:5], v[6:7] op_sel:[1,0]
	s_nop 0
	v_not_b32_e32 v21, v7
	v_or_b32_e32 v25, 0x80000000, v7
	v_cmp_gt_i32_e32 vcc, 0, v7
	s_nop 1
	v_cndmask_b32_e32 v7, v25, v21, vcc
	v_and_b32_e32 v7, 0xffffff00, v7
	v_or_b32_e32 v7, 0xa0, v7
	v_max_u32_e32 v21, v23, v7
	v_med3_u32 v23, v23, v8, v7
	v_med3_u32 v8, v8, v22, v7
	v_med3_u32 v22, v22, v24, v7
	v_med3_u32 v24, v24, v9, v7
	v_med3_u32 v9, v9, v10, v7
	v_med3_u32 v10, v10, v12, v7
	v_med3_u32 v12, v12, v13, v7
	v_med3_u32 v13, v13, v14, v7
	v_med3_u32 v14, v14, v18, v7
	v_med3_u32 v18, v18, v19, v7
	v_med3_u32 v19, v19, v15, v7
	v_med3_u32 v15, v15, v16, v7
	v_med3_u32 v16, v16, v17, v7
	v_med3_u32 v17, v17, v20, v7
	v_min_u32_e32 v7, v20, v7
	v_not_b32_e32 v20, v6
	v_or_b32_e32 v25, 0x80000000, v6
	v_cmp_gt_i32_e32 vcc, 0, v6
	s_nop 1
	v_cndmask_b32_e32 v6, v25, v20, vcc
	v_and_b32_e32 v6, 0xffffff00, v6
	v_or_b32_e32 v6, 0xb0, v6
	v_max_u32_e32 v20, v21, v6
	v_med3_u32 v21, v21, v23, v6
	v_med3_u32 v23, v23, v8, v6
	v_med3_u32 v8, v8, v22, v6
	v_med3_u32 v22, v22, v24, v6
	v_med3_u32 v24, v24, v9, v6
	v_med3_u32 v9, v9, v10, v6
; __device__ __forceinline__ void ins16(uint32_t (&Lk)[16], uint32_t x) {
; #pragma unroll
;   for (int i = 0; i < 16; ++i) { uint32_t hi = max(Lk[i], x); x = min(Lk[i], x); Lk[i] = hi; }
; __device__ void phase_q_route(KParams& p, int bid, int nb, char* smem) {
;     ...
;     for (int a = 0; a < 16; ++a)
; #pragma unroll
;       for (int bq = 0; bq < 16; ++bq)
;         if ((a + 1) * (bq + 1) <= 16) ins16(C, (mono_key(v1[a] + v2[bq]) & ~0xFFu) | (uint32_t)(a * 16 + bq));
;     ...
;     const size_t ob = (size_t)(m0 + w * 32 + l31) * 128 + h * 16;
	v_med3_u32 v10, v10, v12, v6
	v_med3_u32 v12, v12, v13, v6
	v_med3_u32 v13, v13, v14, v6
	v_med3_u32 v14, v14, v18, v6
	v_med3_u32 v18, v18, v19, v6
	v_med3_u32 v19, v19, v15, v6
	v_med3_u32 v15, v15, v16, v6
	v_med3_u32 v16, v16, v17, v6
	v_min_u32_e32 v6, v17, v6
	v_cmp_lt_i32_e32 vcc, -1, v26
	v_max3_u32 v2, v2, v7, v6
	s_nop 0
	v_cndmask_b32_e64 v6, v174, -1, vcc
	v_cmp_lt_i32_e32 vcc, -1, v11
	v_xor_b32_e32 v7, v6, v31
	s_nop 0
	v_cndmask_b32_e64 v11, v174, -1, vcc
	v_xor_b32_e32 v6, v11, v32
	v_pk_add_f32 v[6:7], v[4:5], v[6:7] op_sel:[1,0]
	s_nop 0
	v_not_b32_e32 v11, v7
	v_or_b32_e32 v17, 0x80000000, v7
	v_cmp_gt_i32_e32 vcc, 0, v7
	s_nop 1
	v_cndmask_b32_e32 v7, v17, v11, vcc
	v_and_b32_e32 v7, 0xffffff00, v7
	v_or_b32_e32 v7, 0xc0, v7
	v_max_u32_e32 v11, v20, v7
	v_med3_u32 v17, v20, v21, v7
	v_med3_u32 v20, v21, v23, v7
	v_med3_u32 v21, v23, v8, v7
	v_med3_u32 v8, v8, v22, v7
	v_med3_u32 v22, v22, v24, v7
	v_med3_u32 v23, v24, v9, v7
	v_med3_u32 v9, v9, v10, v7
	v_med3_u32 v10, v10, v12, v7
	v_med3_u32 v12, v12, v13, v7
	v_med3_u32 v13, v13, v14, v7
	v_med3_u32 v14, v14, v18, v7
	v_med3_u32 v18, v18, v19, v7
	v_med3_u32 v19, v19, v15, v7
	v_med3_u32 v15, v15, v16, v7
	v_min_u32_e32 v7, v16, v7
	v_not_b32_e32 v16, v6
	v_or_b32_e32 v24, 0x80000000, v6
	v_cmp_gt_i32_e32 vcc, 0, v6
	s_nop 1
	v_cndmask_b32_e32 v6, v24, v16, vcc
	v_and_b32_e32 v6, 0xffffff00, v6
	v_or_b32_e32 v6, 0xd0, v6
	v_max_u32_e32 v16, v11, v6
	v_med3_u32 v11, v11, v17, v6
	v_med3_u32 v17, v17, v20, v6
	v_med3_u32 v20, v20, v21, v6
	v_med3_u32 v21, v21, v8, v6
	v_med3_u32 v8, v8, v22, v6
	v_med3_u32 v22, v22, v23, v6
	v_med3_u32 v23, v23, v9, v6
	v_med3_u32 v9, v9, v10, v6
	v_med3_u32 v10, v10, v12, v6
	v_med3_u32 v12, v12, v13, v6
	v_med3_u32 v13, v13, v14, v6
	v_med3_u32 v14, v14, v18, v6
	v_med3_u32 v18, v18, v19, v6
	v_med3_u32 v19, v19, v15, v6
	v_min_u32_e32 v6, v15, v6
	v_max3_u32 v24, v2, v7, v6
	v_mov_b32_e32 v2, v4
	v_pk_add_f32 v[2:3], v[4:5], v[2:3] op_sel:[1,0]
	s_nop 0
	v_not_b32_e32 v4, v3
	v_or_b32_e32 v5, 0x80000000, v3
	v_cmp_gt_i32_e32 vcc, 0, v3
	s_nop 1
	v_cndmask_b32_e32 v3, v5, v4, vcc
	v_and_b32_e32 v3, 0xffffff00, v3
	v_or_b32_e32 v3, 0xe0, v3
	v_max_u32_e32 v5, v16, v3
	v_med3_u32 v6, v16, v11, v3
	v_med3_u32 v7, v11, v17, v3
	v_med3_u32 v11, v17, v20, v3
	v_med3_u32 v15, v20, v21, v3
	v_med3_u32 v16, v21, v8, v3
	v_min_u32_e32 v3, v8, v3
	v_not_b32_e32 v4, v2
	v_or_b32_e32 v8, 0x80000000, v2
	v_cmp_gt_i32_e32 vcc, 0, v2
	v_max_u32_e32 v17, v22, v3
	v_min_u32_e32 v3, v22, v3
	v_cndmask_b32_e32 v2, v8, v4, vcc
	v_and_b32_e32 v2, 0xffffff00, v2
	v_or_b32_e32 v2, 0xf0, v2
	v_max_u32_e32 v4, v5, v2
	v_med3_u32 v5, v5, v6, v2
	v_med3_u32 v6, v6, v7, v2
	v_med3_u32 v7, v7, v11, v2
	v_min_u32_e32 v2, v11, v2
	v_max_u32_e32 v20, v23, v3
	v_min_u32_e32 v3, v23, v3
	v_max_u32_e32 v8, v15, v2
	v_min_u32_e32 v2, v15, v2
	v_max_u32_e32 v21, v9, v3
	v_min_u32_e32 v3, v9, v3
	v_max_u32_e32 v9, v16, v2
	v_min_u32_e32 v2, v16, v2
	v_max_u32_e32 v22, v10, v3
	v_min_u32_e32 v3, v10, v3
	v_max_u32_e32 v10, v17, v2
	v_med3_u32 v11, v17, v20, v2
	v_min_u32_e32 v2, v20, v2
	v_max_u32_e32 v23, v12, v3
	v_min_u32_e32 v3, v12, v3
	v_max_u32_e32 v12, v21, v2
	v_min_u32_e32 v2, v21, v2
	v_max_u32_e32 v25, v13, v3
	v_min_u32_e32 v3, v13, v3
	v_max_u32_e32 v13, v22, v2
	v_min_u32_e32 v2, v22, v2
	v_max_u32_e32 v26, v14, v3
	v_min_u32_e32 v3, v14, v3
	v_max_u32_e32 v14, v23, v2
	v_med3_u32 v15, v23, v25, v2
	v_min_u32_e32 v2, v25, v2
	v_max_u32_e32 v27, v18, v3
	v_min_u32_e32 v3, v18, v3
	v_max_u32_e32 v16, v26, v2
	v_min_u32_e32 v2, v26, v2
	v_max_u32_e32 v28, v19, v3
	v_max_u32_e32 v17, v27, v2
	v_min_u32_e32 v2, v27, v2
	v_min_u32_e32 v3, v19, v3
	v_max_u32_e32 v18, v28, v2
	v_min_u32_e32 v2, v28, v2
	v_max3_u32 v19, v24, v3, v2
	v_add_u32_e32 v2, s42, v79
	v_ashrrev_i32_e32 v3, 31, v2
	v_lshlrev_b64 v[2:3], 7, v[2:3]
	v_lshl_or_b32 v2, s50, 4, v2
	s_and_saveexec_b64 s[42:43], s[8:9]
	s_xor_b64 s[42:43], exec, s[42:43]
	s_cbranch_execz .LBB0_1194
; __device__ void phase_q_route(KParams& p, int bid, int nb, char* smem) {
;     ...
;       const uint32_t code = C[r] & 0xFFu;
;       te[r] = (int)(ib[code >> 4] * 128u + ib[16 + (code & 15u)]);
;       ts[r] = unmono_key(C[r] & ~0xFFu);
;     }
;     const float mx = ts[0];
;     float den = 0.f;
; #pragma unroll
;     for (int r = 0; r < 16; ++r) { ts[r] = __expf(ts[r] - mx); den += ts[r]; }
;     const float inv = 1.f / den;
;     const size_t ob = (size_t)(m0 + w * 32 + l31) * 128 + h * 16;
;     if (lh == 0) {
; #pragma unroll
;       for (int r = 0; r < 16; r += 4) *reinterpret_cast<int4*>(p.idx + ob + r) = int4{te[r], te[r + 1], te[r + 2], te[r + 3]};
;     } else {
; #pragma unroll
;       for (int r = 0; r < 16; r += 4)
;         *reinterpret_cast<float4*>(p.gate + ob + r) = float4{ts[r] * inv, ts[r + 1] * inv, ts[r + 2] * inv, ts[r + 3] * inv};
	v_cmp_lt_i32_e32 vcc, -1, v4
	s_nop 1
	v_cndmask_b32_e64 v20, v174, -1, vcc
	v_cmp_lt_i32_e32 vcc, -1, v5
	v_bitop3_b32 v20, v20, v4, s47 bitop3:0x78
	v_sub_f32_e32 v4, v20, v20
	v_cndmask_b32_e64 v21, v174, -1, vcc
	v_cmp_lt_i32_e32 vcc, -1, v6
	v_bitop3_b32 v5, v21, v5, s47 bitop3:0x78
	v_mul_f32_e32 v4, 0x3fb8aa3b, v4
	v_cndmask_b32_e64 v21, v174, -1, vcc
	v_cmp_lt_i32_e32 vcc, -1, v7
	v_sub_f32_e32 v5, v5, v20
	v_bitop3_b32 v6, v21, v6, s47 bitop3:0x78
	v_cndmask_b32_e64 v21, v174, -1, vcc
	v_cmp_lt_i32_e32 vcc, -1, v8
	v_exp_f32_e32 v4, v4
	v_mul_f32_e32 v5, 0x3fb8aa3b, v5
	v_sub_f32_e32 v6, v6, v20
	v_bitop3_b32 v7, v21, v7, s47 bitop3:0x78
	v_cndmask_b32_e64 v22, v174, -1, vcc
	v_cmp_lt_i32_e32 vcc, -1, v9
	v_exp_f32_e32 v5, v5
	v_mul_f32_e32 v6, 0x3fb8aa3b, v6
	v_sub_f32_e32 v7, v7, v20
	v_bitop3_b32 v8, v22, v8, s47 bitop3:0x78
	v_cndmask_b32_e64 v22, v174, -1, vcc
	v_cmp_lt_i32_e32 vcc, -1, v10
	v_exp_f32_e32 v6, v6
	v_mul_f32_e32 v7, 0x3fb8aa3b, v7
	v_sub_f32_e32 v8, v8, v20
	v_bitop3_b32 v9, v22, v9, s47 bitop3:0x78
	v_cndmask_b32_e64 v22, v174, -1, vcc
	v_cmp_lt_i32_e32 vcc, -1, v11
	v_exp_f32_e32 v7, v7
	v_mul_f32_e32 v8, 0x3fb8aa3b, v8
	v_sub_f32_e32 v9, v9, v20
	v_bitop3_b32 v10, v22, v10, s47 bitop3:0x78
	v_cndmask_b32_e64 v22, v174, -1, vcc
	v_cmp_lt_i32_e32 vcc, -1, v12
	v_add_f32_e32 v21, 0, v4
	v_exp_f32_e32 v8, v8
	v_mul_f32_e32 v9, 0x3fb8aa3b, v9
	v_sub_f32_e32 v10, v10, v20
	v_bitop3_b32 v11, v22, v11, s47 bitop3:0x78
	v_cndmask_b32_e64 v22, v174, -1, vcc
	v_cmp_lt_i32_e32 vcc, -1, v13
	v_add_f32_e32 v21, v21, v5
	v_exp_f32_e32 v9, v9
	v_mul_f32_e32 v10, 0x3fb8aa3b, v10
	v_sub_f32_e32 v11, v11, v20
	v_bitop3_b32 v12, v22, v12, s47 bitop3:0x78
	v_cndmask_b32_e64 v22, v174, -1, vcc
	v_cmp_lt_i32_e32 vcc, -1, v14
	v_add_f32_e32 v21, v21, v6
	v_exp_f32_e32 v10, v10
	v_mul_f32_e32 v11, 0x3fb8aa3b, v11
	v_sub_f32_e32 v12, v12, v20
	v_bitop3_b32 v13, v22, v13, s47 bitop3:0x78
	v_cndmask_b32_e64 v22, v174, -1, vcc
	v_cmp_lt_i32_e32 vcc, -1, v15
	v_add_f32_e32 v21, v21, v7
	v_exp_f32_e32 v11, v11
	v_mul_f32_e32 v12, 0x3fb8aa3b, v12
	v_sub_f32_e32 v13, v13, v20
	v_bitop3_b32 v14, v22, v14, s47 bitop3:0x78
	v_cndmask_b32_e64 v22, v174, -1, vcc
	v_cmp_lt_i32_e32 vcc, -1, v16
	v_add_f32_e32 v21, v21, v8
	v_exp_f32_e32 v12, v12
	v_mul_f32_e32 v13, 0x3fb8aa3b, v13
	v_sub_f32_e32 v14, v14, v20
	v_bitop3_b32 v15, v22, v15, s47 bitop3:0x78
	v_cndmask_b32_e64 v22, v174, -1, vcc
	v_cmp_lt_i32_e32 vcc, -1, v17
	v_add_f32_e32 v21, v21, v9
	v_exp_f32_e32 v13, v13
	v_mul_f32_e32 v14, 0x3fb8aa3b, v14
	v_sub_f32_e32 v15, v15, v20
	v_bitop3_b32 v16, v22, v16, s47 bitop3:0x78
	v_cndmask_b32_e64 v22, v174, -1, vcc
	v_cmp_lt_i32_e32 vcc, -1, v18
	v_add_f32_e32 v21, v21, v10
	v_exp_f32_e32 v14, v14
	v_mul_f32_e32 v15, 0x3fb8aa3b, v15
	v_sub_f32_e32 v16, v16, v20
	v_bitop3_b32 v17, v22, v17, s47 bitop3:0x78
	v_cndmask_b32_e64 v22, v174, -1, vcc
	v_cmp_lt_i32_e32 vcc, -1, v19
	v_add_f32_e32 v21, v21, v11
	v_exp_f32_e32 v15, v15
	v_mul_f32_e32 v16, 0x3fb8aa3b, v16
	v_sub_f32_e32 v17, v17, v20
	v_bitop3_b32 v18, v22, v18, s47 bitop3:0x78
	v_cndmask_b32_e64 v22, v174, -1, vcc
	v_add_f32_e32 v21, v21, v12
	v_exp_f32_e32 v16, v16
	v_mul_f32_e32 v17, 0x3fb8aa3b, v17
	v_sub_f32_e32 v18, v18, v20
	v_bitop3_b32 v19, v22, v19, s47 bitop3:0x78
	v_add_f32_e32 v21, v21, v13
	v_exp_f32_e32 v17, v17
	v_mul_f32_e32 v18, 0x3fb8aa3b, v18
	v_sub_f32_e32 v19, v19, v20
	v_add_f32_e32 v21, v21, v14
	v_exp_f32_e32 v18, v18
	v_mul_f32_e32 v19, 0x3fb8aa3b, v19
	v_add_f32_e32 v21, v21, v15
	v_exp_f32_e32 v19, v19
	v_add_f32_e32 v20, v21, v16
	v_add_f32_e32 v20, v20, v17
	v_add_f32_e32 v20, v20, v18
	v_add_f32_e32 v20, v20, v19
	v_div_scale_f32 v21, s[48:49], v20, v20, 1.0
	v_rcp_f32_e32 v22, v21
	s_nop 0
	v_fma_f32 v23, -v21, v22, 1.0
	v_fmac_f32_e32 v22, v23, v22
	v_div_scale_f32 v23, vcc, 1.0, v20, 1.0
	v_mul_f32_e32 v24, v23, v22
	v_fma_f32 v25, -v21, v24, v23
	v_fmac_f32_e32 v24, v25, v22
	v_fma_f32 v21, -v21, v24, v23
	v_div_fmas_f32 v21, v21, v22, v24
	v_div_fixup_f32 v20, v21, v20, 1.0
	v_lshl_add_u64 v[22:23], v[2:3], 2, s[16:17]
	v_pk_mul_f32 v[2:3], v[4:5], v[20:21] op_sel_hi:[1,0]
	v_pk_mul_f32 v[4:5], v[6:7], v[20:21] op_sel_hi:[1,0]
	global_store_dwordx4 v[22:23], v[2:5], off
	s_nop 1
	v_pk_mul_f32 v[2:3], v[8:9], v[20:21] op_sel_hi:[1,0]
	v_pk_mul_f32 v[4:5], v[10:11], v[20:21] op_sel_hi:[1,0]
	global_store_dwordx4 v[22:23], v[2:5], off offset:16
	s_nop 1
	v_pk_mul_f32 v[2:3], v[12:13], v[20:21] op_sel_hi:[1,0]
	v_pk_mul_f32 v[4:5], v[14:15], v[20:21] op_sel_hi:[1,0]
	global_store_dwordx4 v[22:23], v[2:5], off offset:32
	s_nop 1
	v_pk_mul_f32 v[2:3], v[16:17], v[20:21] op_sel_hi:[1,0]
	v_pk_mul_f32 v[4:5], v[18:19], v[20:21] op_sel_hi:[1,0]
	global_store_dwordx4 v[22:23], v[2:5], off offset:48
